# recheck exact-distance pass handles 64 candidates per pass (8 lanes each) so the slowest block needs one pass
# baseline (speedup 1.0000x reference)
.Lcx_doneb:
	s_waitcnt lgkmcnt(0)
	s_barrier
	ds_read_b32 v66, v248
	s_waitcnt lgkmcnt(0)
	v_cmp_ne_u32_e32 vcc, 0, v66
	s_cbranch_vccz .LBB0_447
	v_min_u32_e32 v70, 0x800, v66
	s_lshl_b32 s14, s25, 2
	s_add_i32 s14, s14, 0x21400
	s_mov_b32 s15, 0
	v_lshrrev_b32_e32 v188, 3, v0
	v_and_b32_e32 v189, 7, v0
	v_and_b32_e32 v191, 8, v0
	v_lshl_add_u32 v75, v188, 2, v246
	v_cmp_eq_u32_e64 s[28:29], 0, v189
	v_lshlrev_b32_e32 v190, 4, v189
	v_lshlrev_b32_e32 v191, 4, v191
	v_sub_co_u32_e32 v204, vcc, v170, v191
	s_nop 1
	v_subbrev_co_u32_e32 v205, vcc, 0, v171, vcc
	s_branch .LBB0_443
.LBB0_442:
	s_or_b64 exec, exec, s[0:1]
	s_add_i32 s15, s15, 64
	v_cmp_ge_u32_e32 vcc, s15, v70
	v_add_u32_e32 v75, 0x100, v75
	s_cbranch_vccnz .LBB0_447
.LBB0_443:
	v_add_u32_e32 v66, s15, v188
	v_cmp_lt_u32_e32 vcc, v66, v70
	v_mov_b32_e32 v76, 0
	v_mov_b64_e32 v[66:67], 0
	s_and_saveexec_b64 s[0:1], vcc
	s_cbranch_execz .LBB0_445
	ds_read_b32 v76, v75
	s_waitcnt lgkmcnt(0)
	v_lshrrev_b32_e32 v66, 8, v76
	v_and_b32_e32 v66, 0xfffffc, v66
	v_add_u32_e32 v66, s14, v66
	ds_read_b32 v77, v66
	v_and_b32_e32 v66, 0x3ff, v76
	v_lshl_or_b32 v66, v66, 8, v190
	global_load_dwordx4 v[192:195], v66, s[22:23]
	global_load_dwordx4 v[196:199], v66, s[22:23] offset:128
	s_waitcnt lgkmcnt(0)
	v_add_u32_e32 v168, s24, v77
	v_lshlrev_b64 v[78:79], 8, v[168:169]
	v_lshl_add_u64 v[78:79], v[204:205], 0, v[78:79]
	global_load_dwordx4 v[200:203], v[78:79], off
	global_load_dwordx4 v[240:243], v[78:79], off offset:128
	s_waitcnt vmcnt(2)
	v_cvt_f64_f32_e32 v[208:209], v192
	v_cvt_f64_f32_e32 v[210:211], v193
	v_cvt_f64_f32_e32 v[212:213], v194
	v_cvt_f64_f32_e32 v[214:215], v195
	v_cvt_f64_f32_e32 v[216:217], v196
	v_cvt_f64_f32_e32 v[218:219], v197
	v_cvt_f64_f32_e32 v[220:221], v198
	v_cvt_f64_f32_e32 v[222:223], v199
	s_waitcnt vmcnt(0)
	v_cvt_f64_f32_e32 v[224:225], v200
	v_cvt_f64_f32_e32 v[226:227], v201
	v_cvt_f64_f32_e32 v[228:229], v202
	v_cvt_f64_f32_e32 v[230:231], v203
	v_cvt_f64_f32_e32 v[232:233], v240
	v_cvt_f64_f32_e32 v[234:235], v241
	v_cvt_f64_f32_e32 v[236:237], v242
	v_cvt_f64_f32_e32 v[238:239], v243
	v_add_f64 v[224:225], v[224:225], -v[208:209]
	v_add_f64 v[226:227], v[226:227], -v[210:211]
	v_add_f64 v[228:229], v[228:229], -v[212:213]
	v_add_f64 v[230:231], v[230:231], -v[214:215]
	v_add_f64 v[232:233], v[232:233], -v[216:217]
	v_add_f64 v[234:235], v[234:235], -v[218:219]
	v_add_f64 v[236:237], v[236:237], -v[220:221]
	v_add_f64 v[238:239], v[238:239], -v[222:223]
	v_mul_f64 v[66:67], v[224:225], v[224:225]
	v_fmac_f64_e32 v[66:67], v[226:227], v[226:227]
	v_fmac_f64_e32 v[66:67], v[228:229], v[228:229]
	v_fmac_f64_e32 v[66:67], v[230:231], v[230:231]
	v_fmac_f64_e32 v[66:67], v[232:233], v[232:233]
	v_fmac_f64_e32 v[66:67], v[234:235], v[234:235]
	v_fmac_f64_e32 v[66:67], v[236:237], v[236:237]
	v_fmac_f64_e32 v[66:67], v[238:239], v[238:239]
.LBB0_445:
	s_or_b64 exec, exec, s[0:1]
	s_and_b64 s[16:17], s[28:29], vcc
	s_waitcnt lgkmcnt(0)
	s_nop 3
	v_mov_b32_dpp v68, v66 row_half_mirror row_mask:0xf bank_mask:0xf
	v_mov_b32_dpp v69, v67 row_half_mirror row_mask:0xf bank_mask:0xf
	v_add_f64 v[66:67], v[66:67], v[68:69]
	s_nop 1
	v_mov_b32_dpp v68, v66 quad_perm:[2,3,0,1] row_mask:0xf bank_mask:0xf
	v_mov_b32_dpp v69, v67 quad_perm:[2,3,0,1] row_mask:0xf bank_mask:0xf
	v_add_f64 v[66:67], v[66:67], v[68:69]
	s_nop 1
	v_mov_b32_dpp v68, v66 quad_perm:[1,0,3,2] row_mask:0xf bank_mask:0xf
	v_mov_b32_dpp v69, v67 quad_perm:[1,0,3,2] row_mask:0xf bank_mask:0xf
	v_add_f64 v[66:67], v[66:67], v[68:69]
	s_and_saveexec_b64 s[0:1], s[16:17]
	s_cbranch_execz .LBB0_442
	v_lshrrev_b32_e32 v68, 7, v76
	v_and_b32_e32 v68, 0x1fffff8, v68
	v_bfi_b32 v66, s26, v66, v76
	v_add_u32_e32 v68, 0x21c00, v68
	ds_min_u64 v68, v[66:67]
	s_branch .LBB0_442
